# plus nt on the out-projection's residual-stream stores (16 stores)
# baseline (speedup 1.0000x reference)
.LBB0_526:
	v_lshl_or_b32 v2, s21, 8, v198
	v_lshl_add_u32 v0, s56, 8, v197
	v_ashrrev_i32_e32 v3, 31, v2
	v_lshlrev_b64 v[180:181], 1, v[2:3]
	v_ashrrev_i32_e32 v1, 31, v0
	v_lshl_add_u64 v[2:3], s[44:45], 0, v[180:181]
	v_lshlrev_b64 v[224:225], 11, v[0:1]
	s_nop 15
	s_nop 15
	v_lshl_add_u64 v[4:5], v[2:3], 0, v[224:225]
	global_load_dwordx4 v[200:203], v[4:5], off
	global_load_dwordx4 v[204:207], v[4:5], off offset:2048
	v_or_b32_e32 v4, 16, v0
	v_ashrrev_i32_e32 v5, 31, v4
	v_lshlrev_b64 v[194:195], 11, v[4:5]
	v_lshl_add_u64 v[4:5], v[2:3], 0, v[194:195]
	global_load_dwordx4 v[208:211], v[4:5], off
	global_load_dwordx4 v[212:215], v[4:5], off offset:2048
	s_mov_b64 s[0:1], 0x40000
	v_lshl_add_u64 v[188:189], v[224:225], 0, s[0:1]
	s_mov_b64 s[0:1], 0x48000
	v_or_b32_e32 v4, 32, v0
	v_or_b32_e32 v0, 48, v0
	v_lshl_add_u64 v[186:187], v[224:225], 0, s[0:1]
	s_mov_b64 s[0:1], 0x50000
	v_ashrrev_i32_e32 v5, 31, v4
	v_ashrrev_i32_e32 v1, 31, v0
	v_lshl_add_u64 v[184:185], v[224:225], 0, s[0:1]
	s_mov_b64 s[0:1], 0x58000
	v_lshlrev_b64 v[192:193], 11, v[4:5]
	v_lshlrev_b64 v[190:191], 11, v[0:1]
	v_lshl_add_u64 v[182:183], v[224:225], 0, s[0:1]
	v_lshl_add_u64 v[0:1], v[2:3], 0, v[192:193]
	v_lshl_add_u64 v[4:5], v[2:3], 0, v[190:191]
	v_lshl_add_u64 v[6:7], v[2:3], 0, v[188:189]
	v_lshl_add_u64 v[8:9], v[2:3], 0, v[186:187]
	v_lshl_add_u64 v[10:11], v[2:3], 0, v[184:185]
	v_lshl_add_u64 v[2:3], v[2:3], 0, v[182:183]
	global_load_dwordx4 v[216:219], v[0:1], off
	global_load_dwordx4 v[220:223], v[0:1], off offset:2048
	global_load_dwordx4 v[166:169], v[4:5], off
	global_load_dwordx4 v[162:165], v[4:5], off offset:2048
	global_load_dwordx4 v[28:31], v[6:7], off
	global_load_dwordx4 v[24:27], v[6:7], off offset:2048
	global_load_dwordx4 v[20:23], v[8:9], off
	global_load_dwordx4 v[16:19], v[8:9], off offset:2048
	global_load_dwordx4 v[12:15], v[10:11], off
	s_nop 0
	global_load_dwordx4 v[8:11], v[10:11], off offset:2048
	s_nop 0
	global_load_dwordx4 v[4:7], v[2:3], off
	s_nop 0
	global_load_dwordx4 v[0:3], v[2:3], off offset:2048
	s_andn2_b64 vcc, exec, s[40:41]
	s_mov_b64 s[0:1], -1
	s_waitcnt vmcnt(0)
	v_cndmask_b32_e64 v226, v203, v207, s[38:39]
	v_cndmask_b32_e64 v227, v202, v206, s[38:39]
	v_cndmask_b32_e64 v234, v201, v205, s[38:39]
	v_cndmask_b32_e64 v235, v200, v204, s[38:39]
	v_mov_b32_dpp v227, v227 quad_perm:[1,0,3,2] row_mask:0xf bank_mask:0xf bound_ctrl:1
	v_mov_b32_dpp v234, v234 quad_perm:[1,0,3,2] row_mask:0xf bank_mask:0xf bound_ctrl:1
	v_mov_b32_dpp v235, v235 quad_perm:[1,0,3,2] row_mask:0xf bank_mask:0xf bound_ctrl:1
	v_mov_b32_dpp v226, v226 quad_perm:[1,0,3,2] row_mask:0xf bank_mask:0xf bound_ctrl:1
	v_cndmask_b32_e64 v240, v226, v203, s[38:39]
	v_cndmask_b32_e64 v241, v227, v202, s[38:39]
	v_cndmask_b32_e64 v243, v207, v226, s[38:39]
	v_cndmask_b32_e64 v242, v206, v227, s[38:39]
	v_cndmask_b32_e64 v247, v205, v234, s[38:39]
	v_cndmask_b32_e64 v227, v204, v235, s[38:39]
	v_cndmask_b32_e64 v203, v234, v201, s[38:39]
	v_cndmask_b32_e64 v201, v235, v200, s[38:39]
	v_lshlrev_b32_e32 v204, 16, v241
	v_and_b32_e32 v205, 0xffff0000, v241
	v_lshlrev_b32_e32 v206, 16, v240
	v_and_b32_e32 v207, 0xffff0000, v240
	v_lshlrev_b32_e32 v226, 16, v227
	v_and_b32_e32 v227, 0xffff0000, v227
	v_lshlrev_b32_e32 v234, 16, v247
	v_and_b32_e32 v235, 0xffff0000, v247
	v_lshlrev_b32_e32 v240, 16, v242
	v_and_b32_e32 v241, 0xffff0000, v242
	v_lshlrev_b32_e32 v242, 16, v243
	v_and_b32_e32 v243, 0xffff0000, v243
	v_lshlrev_b32_e32 v200, 16, v201
	v_and_b32_e32 v201, 0xffff0000, v201
	v_lshlrev_b32_e32 v202, 16, v203
	v_and_b32_e32 v203, 0xffff0000, v203
	v_pk_fma_f32 v[156:157], v[156:157], s[90:91], v[206:207] op_sel_hi:[1,0,1]
	v_pk_fma_f32 v[154:155], v[154:155], s[90:91], v[204:205] op_sel_hi:[1,0,1]
	v_pk_fma_f32 v[152:153], v[152:153], s[90:91], v[234:235] op_sel_hi:[1,0,1]
	v_pk_fma_f32 v[150:151], v[150:151], s[90:91], v[226:227] op_sel_hi:[1,0,1]
	v_pk_fma_f32 v[148:149], v[148:149], s[90:91], v[242:243] op_sel_hi:[1,0,1]
	v_pk_fma_f32 v[146:147], v[146:147], s[90:91], v[240:241] op_sel_hi:[1,0,1]
	v_pk_fma_f32 v[160:161], v[160:161], s[90:91], v[202:203] op_sel_hi:[1,0,1]
	v_pk_fma_f32 v[158:159], v[158:159], s[90:91], v[200:201] op_sel_hi:[1,0,1]
	v_cvt_pk_bf16_f32 v154, v154, v155
	v_cvt_pk_bf16_f32 v155, v156, v157
	v_cvt_pk_bf16_f32 v150, v150, v151
	v_cvt_pk_bf16_f32 v151, v152, v153
	v_cvt_pk_bf16_f32 v152, v146, v147
	v_cvt_pk_bf16_f32 v153, v148, v149
	v_cvt_pk_bf16_f32 v158, v158, v159
	v_cvt_pk_bf16_f32 v159, v160, v161
	v_cndmask_b32_e64 v146, v155, v153, s[38:39]
	v_cndmask_b32_e64 v147, v154, v152, s[38:39]
	v_cndmask_b32_e64 v148, v159, v151, s[38:39]
	v_cndmask_b32_e64 v149, v158, v150, s[38:39]
	v_mov_b32_dpp v160, v147 quad_perm:[1,0,3,2] row_mask:0xf bank_mask:0xf bound_ctrl:1
	v_mov_b32_dpp v161, v146 quad_perm:[1,0,3,2] row_mask:0xf bank_mask:0xf bound_ctrl:1
	v_mov_b32_dpp v156, v149 quad_perm:[1,0,3,2] row_mask:0xf bank_mask:0xf bound_ctrl:1
	v_mov_b32_dpp v157, v148 quad_perm:[1,0,3,2] row_mask:0xf bank_mask:0xf bound_ctrl:1
	v_cndmask_b32_e64 v149, v161, v155, s[38:39]
	v_cndmask_b32_e64 v148, v160, v154, s[38:39]
	v_lshl_add_u64 v[154:155], s[44:45], 0, v[224:225]
	v_cndmask_b32_e64 v239, v211, v215, s[38:39]
	v_cndmask_b32_e64 v244, v210, v214, s[38:39]
	v_cndmask_b32_e64 v245, v209, v213, s[38:39]
	v_cndmask_b32_e64 v246, v208, v212, s[38:39]
	v_cndmask_b32_e64 v147, v157, v159, s[38:39]
	v_cndmask_b32_e64 v146, v156, v158, s[38:39]
	v_lshl_add_u64 v[154:155], v[154:155], 0, v[180:181]
	v_cndmask_b32_e64 v153, v153, v161, s[38:39]
	v_cndmask_b32_e64 v152, v152, v160, s[38:39]
	v_cndmask_b32_e64 v151, v151, v157, s[38:39]
	v_cndmask_b32_e64 v150, v150, v156, s[38:39]
	global_store_dwordx4 v[154:155], v[146:149], off nt
	global_store_dwordx4 v[154:155], v[150:153], off offset:2048 nt
	v_cndmask_b32_e64 v200, v219, v223, s[38:39]
	v_mov_b32_dpp v146, v246 quad_perm:[1,0,3,2] row_mask:0xf bank_mask:0xf bound_ctrl:1
	v_mov_b32_dpp v147, v245 quad_perm:[1,0,3,2] row_mask:0xf bank_mask:0xf bound_ctrl:1
	v_mov_b32_dpp v148, v244 quad_perm:[1,0,3,2] row_mask:0xf bank_mask:0xf bound_ctrl:1
	v_mov_b32_dpp v149, v239 quad_perm:[1,0,3,2] row_mask:0xf bank_mask:0xf bound_ctrl:1
	v_cndmask_b32_e64 v153, v149, v211, s[38:39]
	v_cndmask_b32_e64 v151, v148, v210, s[38:39]
	v_cndmask_b32_e64 v150, v147, v209, s[38:39]
	v_cndmask_b32_e64 v152, v146, v208, s[38:39]
	v_cndmask_b32_e64 v161, v215, v149, s[38:39]
	v_cndmask_b32_e64 v159, v214, v148, s[38:39]
	v_cndmask_b32_e64 v157, v213, v147, s[38:39]
	v_cndmask_b32_e64 v155, v212, v146, s[38:39]
	v_lshlrev_b32_e32 v146, 16, v152
	v_and_b32_e32 v147, 0xffff0000, v152
	v_lshlrev_b32_e32 v148, 16, v150
	v_and_b32_e32 v149, 0xffff0000, v150
	v_lshlrev_b32_e32 v150, 16, v151
	v_and_b32_e32 v151, 0xffff0000, v151
	v_lshlrev_b32_e32 v152, 16, v153
	v_and_b32_e32 v153, 0xffff0000, v153
	v_lshlrev_b32_e32 v154, 16, v155
	v_and_b32_e32 v155, 0xffff0000, v155
	v_lshlrev_b32_e32 v156, 16, v157
	v_and_b32_e32 v157, 0xffff0000, v157
	v_lshlrev_b32_e32 v158, 16, v159
	v_and_b32_e32 v159, 0xffff0000, v159
	v_lshlrev_b32_e32 v160, 16, v161
	v_and_b32_e32 v161, 0xffff0000, v161
	v_pk_fma_f32 v[140:141], v[140:141], s[90:91], v[152:153] op_sel_hi:[1,0,1]
	v_pk_fma_f32 v[138:139], v[138:139], s[90:91], v[150:151] op_sel_hi:[1,0,1]
	v_pk_fma_f32 v[136:137], v[136:137], s[90:91], v[156:157] op_sel_hi:[1,0,1]
	v_pk_fma_f32 v[134:135], v[134:135], s[90:91], v[154:155] op_sel_hi:[1,0,1]
	v_pk_fma_f32 v[132:133], v[132:133], s[90:91], v[160:161] op_sel_hi:[1,0,1]
	v_pk_fma_f32 v[130:131], v[130:131], s[90:91], v[158:159] op_sel_hi:[1,0,1]
	v_pk_fma_f32 v[144:145], v[144:145], s[90:91], v[148:149] op_sel_hi:[1,0,1]
	v_pk_fma_f32 v[142:143], v[142:143], s[90:91], v[146:147] op_sel_hi:[1,0,1]
	v_cvt_pk_bf16_f32 v138, v138, v139
	v_cvt_pk_bf16_f32 v139, v140, v141
	v_cvt_pk_bf16_f32 v134, v134, v135
	v_cvt_pk_bf16_f32 v135, v136, v137
	v_cvt_pk_bf16_f32 v136, v130, v131
	v_cvt_pk_bf16_f32 v137, v132, v133
	v_cvt_pk_bf16_f32 v142, v142, v143
	v_cvt_pk_bf16_f32 v143, v144, v145
	v_cndmask_b32_e64 v130, v139, v137, s[38:39]
	v_cndmask_b32_e64 v131, v138, v136, s[38:39]
	v_cndmask_b32_e64 v132, v143, v135, s[38:39]
	v_cndmask_b32_e64 v133, v142, v134, s[38:39]
	v_mov_b32_dpp v144, v131 quad_perm:[1,0,3,2] row_mask:0xf bank_mask:0xf bound_ctrl:1
	v_mov_b32_dpp v145, v130 quad_perm:[1,0,3,2] row_mask:0xf bank_mask:0xf bound_ctrl:1
	v_mov_b32_dpp v140, v133 quad_perm:[1,0,3,2] row_mask:0xf bank_mask:0xf bound_ctrl:1
	v_mov_b32_dpp v141, v132 quad_perm:[1,0,3,2] row_mask:0xf bank_mask:0xf bound_ctrl:1
	v_cndmask_b32_e64 v133, v145, v139, s[38:39]
	v_cndmask_b32_e64 v132, v144, v138, s[38:39]
	v_lshl_add_u64 v[138:139], s[44:45], 0, v[194:195]
	v_cndmask_b32_e64 v201, v218, v222, s[38:39]
	v_cndmask_b32_e64 v202, v217, v221, s[38:39]
	v_cndmask_b32_e64 v203, v216, v220, s[38:39]
	v_cndmask_b32_e64 v131, v141, v143, s[38:39]
	v_cndmask_b32_e64 v130, v140, v142, s[38:39]
	v_lshl_add_u64 v[138:139], v[138:139], 0, v[180:181]
	v_cndmask_b32_e64 v137, v137, v145, s[38:39]
	v_cndmask_b32_e64 v136, v136, v144, s[38:39]
	v_cndmask_b32_e64 v135, v135, v141, s[38:39]
	v_cndmask_b32_e64 v134, v134, v140, s[38:39]
	global_store_dwordx4 v[138:139], v[130:133], off nt
	v_mov_b32_e32 v150, 0
	v_mov_b32_e32 v151, 0
	v_mov_b32_e32 v152, 0
	v_mov_b32_e32 v153, 0
	v_mov_b32_e32 v154, 0
	v_mov_b32_e32 v155, 0
	v_mov_b32_e32 v156, 0
	v_mov_b32_e32 v157, 0
	v_mov_b32_e32 v158, 0
	v_mov_b32_e32 v159, 0
	v_mov_b32_e32 v160, 0
	v_mov_b32_e32 v161, 0
	global_store_dwordx4 v[138:139], v[134:137], off offset:2048 nt
	v_cndmask_b32_e64 v146, v169, v165, s[38:39]
	v_mov_b32_dpp v130, v203 quad_perm:[1,0,3,2] row_mask:0xf bank_mask:0xf bound_ctrl:1
	v_mov_b32_dpp v131, v202 quad_perm:[1,0,3,2] row_mask:0xf bank_mask:0xf bound_ctrl:1
	v_mov_b32_dpp v132, v201 quad_perm:[1,0,3,2] row_mask:0xf bank_mask:0xf bound_ctrl:1
	v_mov_b32_dpp v133, v200 quad_perm:[1,0,3,2] row_mask:0xf bank_mask:0xf bound_ctrl:1
	v_cndmask_b32_e64 v137, v133, v219, s[38:39]
	v_cndmask_b32_e64 v135, v132, v218, s[38:39]
	v_cndmask_b32_e64 v134, v131, v217, s[38:39]
	v_cndmask_b32_e64 v136, v130, v216, s[38:39]
	v_cndmask_b32_e64 v145, v223, v133, s[38:39]
	v_cndmask_b32_e64 v143, v222, v132, s[38:39]
	v_cndmask_b32_e64 v141, v221, v131, s[38:39]
	v_cndmask_b32_e64 v139, v220, v130, s[38:39]
	v_lshlrev_b32_e32 v130, 16, v136
	v_and_b32_e32 v131, 0xffff0000, v136
	v_lshlrev_b32_e32 v132, 16, v134
	v_and_b32_e32 v133, 0xffff0000, v134
	v_lshlrev_b32_e32 v134, 16, v135
	v_and_b32_e32 v135, 0xffff0000, v135
	v_lshlrev_b32_e32 v136, 16, v137
	v_and_b32_e32 v137, 0xffff0000, v137
	v_lshlrev_b32_e32 v138, 16, v139
	v_and_b32_e32 v139, 0xffff0000, v139
	v_lshlrev_b32_e32 v140, 16, v141
	v_and_b32_e32 v141, 0xffff0000, v141
	v_lshlrev_b32_e32 v142, 16, v143
	v_and_b32_e32 v143, 0xffff0000, v143
	v_lshlrev_b32_e32 v144, 16, v145
	v_and_b32_e32 v145, 0xffff0000, v145
	v_pk_fma_f32 v[124:125], v[124:125], s[90:91], v[136:137] op_sel_hi:[1,0,1]
	v_pk_fma_f32 v[122:123], v[122:123], s[90:91], v[134:135] op_sel_hi:[1,0,1]
	v_pk_fma_f32 v[120:121], v[120:121], s[90:91], v[140:141] op_sel_hi:[1,0,1]
	v_pk_fma_f32 v[118:119], v[118:119], s[90:91], v[138:139] op_sel_hi:[1,0,1]
	v_pk_fma_f32 v[116:117], v[116:117], s[90:91], v[144:145] op_sel_hi:[1,0,1]
	v_pk_fma_f32 v[114:115], v[114:115], s[90:91], v[142:143] op_sel_hi:[1,0,1]
	v_pk_fma_f32 v[128:129], v[128:129], s[90:91], v[132:133] op_sel_hi:[1,0,1]
	v_pk_fma_f32 v[126:127], v[126:127], s[90:91], v[130:131] op_sel_hi:[1,0,1]
	v_cvt_pk_bf16_f32 v122, v122, v123
	v_cvt_pk_bf16_f32 v123, v124, v125
	v_cvt_pk_bf16_f32 v118, v118, v119
	v_cvt_pk_bf16_f32 v119, v120, v121
	v_cvt_pk_bf16_f32 v120, v114, v115
	v_cvt_pk_bf16_f32 v121, v116, v117
	v_cvt_pk_bf16_f32 v126, v126, v127
	v_cvt_pk_bf16_f32 v127, v128, v129
	v_cndmask_b32_e64 v114, v123, v121, s[38:39]
	v_cndmask_b32_e64 v115, v122, v120, s[38:39]
	v_cndmask_b32_e64 v116, v127, v119, s[38:39]
	v_cndmask_b32_e64 v117, v126, v118, s[38:39]
	v_mov_b32_dpp v128, v115 quad_perm:[1,0,3,2] row_mask:0xf bank_mask:0xf bound_ctrl:1
	v_mov_b32_dpp v129, v114 quad_perm:[1,0,3,2] row_mask:0xf bank_mask:0xf bound_ctrl:1
	v_mov_b32_dpp v124, v117 quad_perm:[1,0,3,2] row_mask:0xf bank_mask:0xf bound_ctrl:1
	v_mov_b32_dpp v125, v116 quad_perm:[1,0,3,2] row_mask:0xf bank_mask:0xf bound_ctrl:1
	v_cndmask_b32_e64 v117, v129, v123, s[38:39]
	v_cndmask_b32_e64 v116, v128, v122, s[38:39]
	v_lshl_add_u64 v[122:123], s[44:45], 0, v[192:193]
	v_cndmask_b32_e64 v147, v168, v164, s[38:39]
	v_cndmask_b32_e64 v148, v167, v163, s[38:39]
	v_cndmask_b32_e64 v149, v166, v162, s[38:39]
	v_cndmask_b32_e64 v115, v125, v127, s[38:39]
	v_cndmask_b32_e64 v114, v124, v126, s[38:39]
	v_lshl_add_u64 v[122:123], v[122:123], 0, v[180:181]
	v_cndmask_b32_e64 v121, v121, v129, s[38:39]
	v_cndmask_b32_e64 v120, v120, v128, s[38:39]
	v_cndmask_b32_e64 v119, v119, v125, s[38:39]
	v_cndmask_b32_e64 v118, v118, v124, s[38:39]
	global_store_dwordx4 v[122:123], v[114:117], off nt
	v_mov_b32_e32 v134, 0
	v_mov_b32_e32 v135, 0
	v_mov_b32_e32 v136, 0
	v_mov_b32_e32 v137, 0
	v_mov_b32_e32 v138, 0
	v_mov_b32_e32 v139, 0
	v_mov_b32_e32 v140, 0
	v_mov_b32_e32 v141, 0
	v_mov_b32_e32 v142, 0
	v_mov_b32_e32 v143, 0
	v_mov_b32_e32 v144, 0
	v_mov_b32_e32 v145, 0
	global_store_dwordx4 v[122:123], v[118:121], off offset:2048 nt
	v_cndmask_b32_e64 v131, v30, v26, s[38:39]
	v_mov_b32_dpp v114, v149 quad_perm:[1,0,3,2] row_mask:0xf bank_mask:0xf bound_ctrl:1
	v_mov_b32_dpp v115, v148 quad_perm:[1,0,3,2] row_mask:0xf bank_mask:0xf bound_ctrl:1
	v_mov_b32_dpp v116, v147 quad_perm:[1,0,3,2] row_mask:0xf bank_mask:0xf bound_ctrl:1
	v_mov_b32_dpp v117, v146 quad_perm:[1,0,3,2] row_mask:0xf bank_mask:0xf bound_ctrl:1
	v_cndmask_b32_e64 v121, v117, v169, s[38:39]
	v_cndmask_b32_e64 v119, v116, v168, s[38:39]
	v_cndmask_b32_e64 v118, v115, v167, s[38:39]
	v_cndmask_b32_e64 v120, v114, v166, s[38:39]
	v_cndmask_b32_e64 v129, v165, v117, s[38:39]
	v_cndmask_b32_e64 v127, v164, v116, s[38:39]
	v_cndmask_b32_e64 v125, v163, v115, s[38:39]
	v_cndmask_b32_e64 v123, v162, v114, s[38:39]
	v_lshlrev_b32_e32 v114, 16, v120
	v_and_b32_e32 v115, 0xffff0000, v120
	v_lshlrev_b32_e32 v116, 16, v118
	v_and_b32_e32 v117, 0xffff0000, v118
	v_lshlrev_b32_e32 v118, 16, v119
	v_and_b32_e32 v119, 0xffff0000, v119
	v_lshlrev_b32_e32 v120, 16, v121
	v_and_b32_e32 v121, 0xffff0000, v121
	v_lshlrev_b32_e32 v122, 16, v123
	v_and_b32_e32 v123, 0xffff0000, v123
	v_lshlrev_b32_e32 v124, 16, v125
	v_and_b32_e32 v125, 0xffff0000, v125
	v_lshlrev_b32_e32 v126, 16, v127
	v_and_b32_e32 v127, 0xffff0000, v127
	v_lshlrev_b32_e32 v128, 16, v129
	v_and_b32_e32 v129, 0xffff0000, v129
	v_pk_fma_f32 v[108:109], v[108:109], s[90:91], v[120:121] op_sel_hi:[1,0,1]
	v_pk_fma_f32 v[106:107], v[106:107], s[90:91], v[118:119] op_sel_hi:[1,0,1]
	v_pk_fma_f32 v[104:105], v[104:105], s[90:91], v[124:125] op_sel_hi:[1,0,1]
	v_pk_fma_f32 v[102:103], v[102:103], s[90:91], v[122:123] op_sel_hi:[1,0,1]
	v_pk_fma_f32 v[100:101], v[100:101], s[90:91], v[128:129] op_sel_hi:[1,0,1]
	v_pk_fma_f32 v[98:99], v[98:99], s[90:91], v[126:127] op_sel_hi:[1,0,1]
	v_pk_fma_f32 v[112:113], v[112:113], s[90:91], v[116:117] op_sel_hi:[1,0,1]
	v_pk_fma_f32 v[110:111], v[110:111], s[90:91], v[114:115] op_sel_hi:[1,0,1]
	v_cvt_pk_bf16_f32 v106, v106, v107
	v_cvt_pk_bf16_f32 v107, v108, v109
	v_cvt_pk_bf16_f32 v102, v102, v103
	v_cvt_pk_bf16_f32 v103, v104, v105
	v_cvt_pk_bf16_f32 v104, v98, v99
	v_cvt_pk_bf16_f32 v105, v100, v101
	v_cvt_pk_bf16_f32 v110, v110, v111
	v_cvt_pk_bf16_f32 v111, v112, v113
	v_cndmask_b32_e64 v98, v107, v105, s[38:39]
	v_cndmask_b32_e64 v99, v106, v104, s[38:39]
	v_cndmask_b32_e64 v100, v111, v103, s[38:39]
	v_cndmask_b32_e64 v101, v110, v102, s[38:39]
	v_mov_b32_dpp v112, v99 quad_perm:[1,0,3,2] row_mask:0xf bank_mask:0xf bound_ctrl:1
	v_mov_b32_dpp v113, v98 quad_perm:[1,0,3,2] row_mask:0xf bank_mask:0xf bound_ctrl:1
	v_mov_b32_dpp v108, v101 quad_perm:[1,0,3,2] row_mask:0xf bank_mask:0xf bound_ctrl:1
	v_mov_b32_dpp v109, v100 quad_perm:[1,0,3,2] row_mask:0xf bank_mask:0xf bound_ctrl:1
	v_cndmask_b32_e64 v101, v113, v107, s[38:39]
	v_cndmask_b32_e64 v100, v112, v106, s[38:39]
	v_lshl_add_u64 v[106:107], s[44:45], 0, v[190:191]
	v_cndmask_b32_e64 v132, v29, v25, s[38:39]
	v_cndmask_b32_e64 v133, v28, v24, s[38:39]
	v_cndmask_b32_e64 v99, v109, v111, s[38:39]
	v_cndmask_b32_e64 v98, v108, v110, s[38:39]
	v_lshl_add_u64 v[106:107], v[106:107], 0, v[180:181]
	v_cndmask_b32_e64 v130, v31, v27, s[38:39]
	v_cndmask_b32_e64 v105, v105, v113, s[38:39]
	v_cndmask_b32_e64 v104, v104, v112, s[38:39]
	v_cndmask_b32_e64 v103, v103, v109, s[38:39]
	v_cndmask_b32_e64 v102, v102, v108, s[38:39]
	global_store_dwordx4 v[106:107], v[98:101], off nt
	v_mov_b32_e32 v110, 0
	v_mov_b32_e32 v111, 0
	v_mov_b32_e32 v112, 0
	v_mov_b32_e32 v113, 0
	v_mov_b32_e32 v114, 0
	v_mov_b32_e32 v115, 0
	v_mov_b32_e32 v116, 0
	v_mov_b32_e32 v117, 0
	v_mov_b32_e32 v118, 0
	v_mov_b32_e32 v119, 0
	v_mov_b32_e32 v120, 0
	v_mov_b32_e32 v121, 0
	v_mov_b32_e32 v122, 0
	v_mov_b32_e32 v123, 0
	v_mov_b32_e32 v124, 0
	v_mov_b32_e32 v125, 0
	v_mov_b32_e32 v126, 0
	v_mov_b32_e32 v127, 0
	v_mov_b32_e32 v128, 0
	v_mov_b32_e32 v129, 0
	v_mov_b32_e32 v146, 0
	v_mov_b32_e32 v147, 0
	v_mov_b32_e32 v148, 0
	v_mov_b32_e32 v149, 0
	global_store_dwordx4 v[106:107], v[102:105], off offset:2048 nt
	v_cndmask_b32_e64 v107, v22, v18, s[38:39]
	v_mov_b32_dpp v98, v133 quad_perm:[1,0,3,2] row_mask:0xf bank_mask:0xf bound_ctrl:1
	v_mov_b32_dpp v99, v132 quad_perm:[1,0,3,2] row_mask:0xf bank_mask:0xf bound_ctrl:1
	v_mov_b32_dpp v100, v131 quad_perm:[1,0,3,2] row_mask:0xf bank_mask:0xf bound_ctrl:1
	v_mov_b32_dpp v101, v130 quad_perm:[1,0,3,2] row_mask:0xf bank_mask:0xf bound_ctrl:1
	v_cndmask_b32_e64 v30, v100, v30, s[38:39]
	v_cndmask_b32_e64 v29, v99, v29, s[38:39]
	v_cndmask_b32_e64 v28, v98, v28, s[38:39]
	v_cndmask_b32_e64 v31, v101, v31, s[38:39]
	v_cndmask_b32_e64 v105, v27, v101, s[38:39]
	v_cndmask_b32_e64 v103, v26, v100, s[38:39]
	v_cndmask_b32_e64 v101, v25, v99, s[38:39]
	v_cndmask_b32_e64 v99, v24, v98, s[38:39]
	v_lshlrev_b32_e32 v24, 16, v28
	v_and_b32_e32 v25, 0xffff0000, v28
	v_lshlrev_b32_e32 v26, 16, v29
	v_and_b32_e32 v27, 0xffff0000, v29
	v_lshlrev_b32_e32 v28, 16, v30
	v_and_b32_e32 v29, 0xffff0000, v30
	v_lshlrev_b32_e32 v30, 16, v31
	v_and_b32_e32 v31, 0xffff0000, v31
	v_lshlrev_b32_e32 v98, 16, v99
	v_and_b32_e32 v99, 0xffff0000, v99
	v_lshlrev_b32_e32 v100, 16, v101
	v_and_b32_e32 v101, 0xffff0000, v101
	v_lshlrev_b32_e32 v104, 16, v105
	v_and_b32_e32 v105, 0xffff0000, v105
	v_pk_fma_f32 v[26:27], v[96:97], s[90:91], v[26:27] op_sel_hi:[1,0,1]
	v_pk_fma_f32 v[24:25], v[94:95], s[90:91], v[24:25] op_sel_hi:[1,0,1]
	v_pk_fma_f32 v[28:29], v[90:91], s[90:91], v[28:29] op_sel_hi:[1,0,1]
	v_lshlrev_b32_e32 v102, 16, v103
	v_and_b32_e32 v103, 0xffff0000, v103
	v_pk_fma_f32 v[30:31], v[92:93], s[90:91], v[30:31] op_sel_hi:[1,0,1]
	v_cvt_pk_bf16_f32 v90, v24, v25
	v_cvt_pk_bf16_f32 v91, v26, v27
	v_cvt_pk_bf16_f32 v92, v28, v29
	v_pk_fma_f32 v[24:25], v[88:89], s[90:91], v[100:101] op_sel_hi:[1,0,1]
	v_pk_fma_f32 v[26:27], v[86:87], s[90:91], v[98:99] op_sel_hi:[1,0,1]
	v_pk_fma_f32 v[28:29], v[84:85], s[90:91], v[104:105] op_sel_hi:[1,0,1]
	v_cvt_pk_bf16_f32 v93, v30, v31
	v_pk_fma_f32 v[30:31], v[82:83], s[90:91], v[102:103] op_sel_hi:[1,0,1]
	v_cvt_pk_bf16_f32 v82, v26, v27
	v_cvt_pk_bf16_f32 v83, v24, v25
	v_cvt_pk_bf16_f32 v28, v28, v29
	v_cvt_pk_bf16_f32 v30, v30, v31
	v_cndmask_b32_e64 v24, v93, v28, s[38:39]
	v_cndmask_b32_e64 v26, v91, v83, s[38:39]
	v_cndmask_b32_e64 v27, v90, v82, s[38:39]
	v_cndmask_b32_e64 v25, v92, v30, s[38:39]
	v_mov_b32_dpp v29, v26 quad_perm:[1,0,3,2] row_mask:0xf bank_mask:0xf bound_ctrl:1
	v_mov_b32_dpp v84, v27 quad_perm:[1,0,3,2] row_mask:0xf bank_mask:0xf bound_ctrl:1
	v_mov_b32_dpp v31, v24 quad_perm:[1,0,3,2] row_mask:0xf bank_mask:0xf bound_ctrl:1
	v_mov_b32_dpp v85, v25 quad_perm:[1,0,3,2] row_mask:0xf bank_mask:0xf bound_ctrl:1
	v_cndmask_b32_e64 v27, v31, v93, s[38:39]
	v_cndmask_b32_e64 v25, v29, v91, s[38:39]
	v_cndmask_b32_e64 v31, v28, v31, s[38:39]
	v_cndmask_b32_e64 v29, v83, v29, s[38:39]
	v_cndmask_b32_e64 v28, v82, v84, s[38:39]
	v_lshl_add_u64 v[82:83], s[44:45], 0, v[188:189]
	v_cndmask_b32_e64 v108, v21, v17, s[38:39]
	v_cndmask_b32_e64 v109, v20, v16, s[38:39]
	v_cndmask_b32_e64 v26, v85, v92, s[38:39]
	v_cndmask_b32_e64 v24, v84, v90, s[38:39]
	v_lshl_add_u64 v[82:83], v[82:83], 0, v[180:181]
	v_cndmask_b32_e64 v106, v23, v19, s[38:39]
	v_cndmask_b32_e64 v30, v30, v85, s[38:39]
	global_store_dwordx4 v[82:83], v[24:27], off nt
	v_mov_b32_e32 v86, 0
	v_mov_b32_e32 v87, 0
	v_mov_b32_e32 v88, 0
	v_mov_b32_e32 v89, 0
	v_mov_b32_e32 v90, 0
	v_mov_b32_e32 v91, 0
	v_mov_b32_e32 v92, 0
	v_mov_b32_e32 v93, 0
	v_mov_b32_e32 v94, 0
	v_mov_b32_e32 v95, 0
	v_mov_b32_e32 v96, 0
	v_mov_b32_e32 v97, 0
	v_mov_b32_e32 v98, 0
	v_mov_b32_e32 v99, 0
	v_mov_b32_e32 v100, 0
	v_mov_b32_e32 v101, 0
	v_mov_b32_e32 v102, 0
	v_mov_b32_e32 v103, 0
	v_mov_b32_e32 v104, 0
	v_mov_b32_e32 v105, 0
	v_mov_b32_e32 v130, 0
	v_mov_b32_e32 v131, 0
	v_mov_b32_e32 v132, 0
	v_mov_b32_e32 v133, 0
	global_store_dwordx4 v[82:83], v[28:31], off offset:2048 nt
	v_cndmask_b32_e64 v83, v14, v10, s[38:39]
	v_mov_b32_dpp v24, v109 quad_perm:[1,0,3,2] row_mask:0xf bank_mask:0xf bound_ctrl:1
	v_mov_b32_dpp v25, v108 quad_perm:[1,0,3,2] row_mask:0xf bank_mask:0xf bound_ctrl:1
	v_mov_b32_dpp v26, v107 quad_perm:[1,0,3,2] row_mask:0xf bank_mask:0xf bound_ctrl:1
	v_mov_b32_dpp v27, v106 quad_perm:[1,0,3,2] row_mask:0xf bank_mask:0xf bound_ctrl:1
	v_cndmask_b32_e64 v22, v26, v22, s[38:39]
	v_cndmask_b32_e64 v21, v25, v21, s[38:39]
	v_cndmask_b32_e64 v20, v24, v20, s[38:39]
	v_cndmask_b32_e64 v23, v27, v23, s[38:39]
	v_cndmask_b32_e64 v31, v19, v27, s[38:39]
	v_cndmask_b32_e64 v29, v18, v26, s[38:39]
	v_cndmask_b32_e64 v27, v17, v25, s[38:39]
	v_cndmask_b32_e64 v25, v16, v24, s[38:39]
	v_lshlrev_b32_e32 v16, 16, v20
	v_and_b32_e32 v17, 0xffff0000, v20
	v_lshlrev_b32_e32 v18, 16, v21
	v_and_b32_e32 v19, 0xffff0000, v21
	v_lshlrev_b32_e32 v20, 16, v22
	v_and_b32_e32 v21, 0xffff0000, v22
	v_lshlrev_b32_e32 v22, 16, v23
	v_and_b32_e32 v23, 0xffff0000, v23
	v_lshlrev_b32_e32 v24, 16, v25
	v_and_b32_e32 v25, 0xffff0000, v25
	v_lshlrev_b32_e32 v26, 16, v27
	v_and_b32_e32 v27, 0xffff0000, v27
	v_lshlrev_b32_e32 v30, 16, v31
	v_and_b32_e32 v31, 0xffff0000, v31
	v_pk_fma_f32 v[18:19], v[80:81], s[90:91], v[18:19] op_sel_hi:[1,0,1]
	v_pk_fma_f32 v[16:17], v[78:79], s[90:91], v[16:17] op_sel_hi:[1,0,1]
	v_pk_fma_f32 v[20:21], v[74:75], s[90:91], v[20:21] op_sel_hi:[1,0,1]
	v_lshlrev_b32_e32 v28, 16, v29
	v_and_b32_e32 v29, 0xffff0000, v29
	v_pk_fma_f32 v[22:23], v[76:77], s[90:91], v[22:23] op_sel_hi:[1,0,1]
	v_cvt_pk_bf16_f32 v74, v16, v17
	v_cvt_pk_bf16_f32 v75, v18, v19
	v_cvt_pk_bf16_f32 v76, v20, v21
	v_pk_fma_f32 v[16:17], v[64:65], s[90:91], v[26:27] op_sel_hi:[1,0,1]
	v_pk_fma_f32 v[18:19], v[62:63], s[90:91], v[24:25] op_sel_hi:[1,0,1]
	v_pk_fma_f32 v[20:21], v[60:61], s[90:91], v[30:31] op_sel_hi:[1,0,1]
	v_cvt_pk_bf16_f32 v77, v22, v23
	v_pk_fma_f32 v[22:23], v[58:59], s[90:91], v[28:29] op_sel_hi:[1,0,1]
	v_cvt_pk_bf16_f32 v24, v18, v19
	v_cvt_pk_bf16_f32 v25, v16, v17
	v_cvt_pk_bf16_f32 v20, v20, v21
	v_cvt_pk_bf16_f32 v22, v22, v23
	v_cndmask_b32_e64 v16, v77, v20, s[38:39]
	v_cndmask_b32_e64 v18, v75, v25, s[38:39]
	v_cndmask_b32_e64 v19, v74, v24, s[38:39]
	v_cndmask_b32_e64 v17, v76, v22, s[38:39]
	v_mov_b32_dpp v21, v18 quad_perm:[1,0,3,2] row_mask:0xf bank_mask:0xf bound_ctrl:1
	v_mov_b32_dpp v26, v19 quad_perm:[1,0,3,2] row_mask:0xf bank_mask:0xf bound_ctrl:1
	v_mov_b32_dpp v23, v16 quad_perm:[1,0,3,2] row_mask:0xf bank_mask:0xf bound_ctrl:1
	v_mov_b32_dpp v27, v17 quad_perm:[1,0,3,2] row_mask:0xf bank_mask:0xf bound_ctrl:1
	v_cndmask_b32_e64 v19, v23, v77, s[38:39]
	v_cndmask_b32_e64 v17, v21, v75, s[38:39]
	v_cndmask_b32_e64 v23, v20, v23, s[38:39]
	v_cndmask_b32_e64 v21, v25, v21, s[38:39]
	v_cndmask_b32_e64 v20, v24, v26, s[38:39]
	v_lshl_add_u64 v[24:25], s[44:45], 0, v[186:187]
	v_cndmask_b32_e64 v84, v13, v9, s[38:39]
	v_cndmask_b32_e64 v85, v12, v8, s[38:39]
	v_cndmask_b32_e64 v18, v27, v76, s[38:39]
	v_cndmask_b32_e64 v16, v26, v74, s[38:39]
	v_lshl_add_u64 v[24:25], v[24:25], 0, v[180:181]
	v_cndmask_b32_e64 v82, v15, v11, s[38:39]
	v_cndmask_b32_e64 v22, v22, v27, s[38:39]
	global_store_dwordx4 v[24:25], v[16:19], off nt
	v_mov_b32_e32 v58, 0
	v_mov_b32_e32 v59, 0
	v_mov_b32_e32 v60, 0
	v_mov_b32_e32 v61, 0
	v_mov_b32_e32 v62, 0
	v_mov_b32_e32 v63, 0
	v_mov_b32_e32 v64, 0
	v_mov_b32_e32 v65, 0
	v_mov_b32_e32 v74, 0
	v_mov_b32_e32 v75, 0
	v_mov_b32_e32 v76, 0
	v_mov_b32_e32 v77, 0
	v_mov_b32_e32 v78, 0
	v_mov_b32_e32 v79, 0
	v_mov_b32_e32 v80, 0
	v_mov_b32_e32 v81, 0
	v_mov_b32_e32 v106, 0
	v_mov_b32_e32 v107, 0
	v_mov_b32_e32 v108, 0
	v_mov_b32_e32 v109, 0
	global_store_dwordx4 v[24:25], v[20:23], off offset:2048 nt
	v_cndmask_b32_e64 v25, v6, v2, s[38:39]
	v_mov_b32_dpp v16, v85 quad_perm:[1,0,3,2] row_mask:0xf bank_mask:0xf bound_ctrl:1
	v_mov_b32_dpp v17, v84 quad_perm:[1,0,3,2] row_mask:0xf bank_mask:0xf bound_ctrl:1
	v_mov_b32_dpp v18, v83 quad_perm:[1,0,3,2] row_mask:0xf bank_mask:0xf bound_ctrl:1
	v_mov_b32_dpp v19, v82 quad_perm:[1,0,3,2] row_mask:0xf bank_mask:0xf bound_ctrl:1
	v_cndmask_b32_e64 v14, v18, v14, s[38:39]
	v_cndmask_b32_e64 v13, v17, v13, s[38:39]
	v_cndmask_b32_e64 v12, v16, v12, s[38:39]
	v_cndmask_b32_e64 v15, v19, v15, s[38:39]
	v_cndmask_b32_e64 v23, v11, v19, s[38:39]
	v_cndmask_b32_e64 v21, v10, v18, s[38:39]
	v_cndmask_b32_e64 v19, v9, v17, s[38:39]
	v_cndmask_b32_e64 v17, v8, v16, s[38:39]
	v_lshlrev_b32_e32 v8, 16, v12
	v_and_b32_e32 v9, 0xffff0000, v12
	v_lshlrev_b32_e32 v10, 16, v13
	v_and_b32_e32 v11, 0xffff0000, v13
	v_lshlrev_b32_e32 v12, 16, v14
	v_and_b32_e32 v13, 0xffff0000, v14
	v_lshlrev_b32_e32 v14, 16, v15
	v_and_b32_e32 v15, 0xffff0000, v15
	v_lshlrev_b32_e32 v16, 16, v17
	v_and_b32_e32 v17, 0xffff0000, v17
	v_lshlrev_b32_e32 v18, 16, v19
	v_and_b32_e32 v19, 0xffff0000, v19
	v_lshlrev_b32_e32 v22, 16, v23
	v_and_b32_e32 v23, 0xffff0000, v23
	v_pk_fma_f32 v[10:11], v[56:57], s[90:91], v[10:11] op_sel_hi:[1,0,1]
	v_pk_fma_f32 v[8:9], v[54:55], s[90:91], v[8:9] op_sel_hi:[1,0,1]
	v_pk_fma_f32 v[12:13], v[50:51], s[90:91], v[12:13] op_sel_hi:[1,0,1]
	v_lshlrev_b32_e32 v20, 16, v21
	v_and_b32_e32 v21, 0xffff0000, v21
	v_pk_fma_f32 v[14:15], v[52:53], s[90:91], v[14:15] op_sel_hi:[1,0,1]
	v_cvt_pk_bf16_f32 v28, v8, v9
	v_cvt_pk_bf16_f32 v29, v10, v11
	v_cvt_pk_bf16_f32 v30, v12, v13
	v_pk_fma_f32 v[8:9], v[72:73], s[90:91], v[18:19] op_sel_hi:[1,0,1]
	v_pk_fma_f32 v[10:11], v[70:71], s[90:91], v[16:17] op_sel_hi:[1,0,1]
	v_pk_fma_f32 v[12:13], v[68:69], s[90:91], v[22:23] op_sel_hi:[1,0,1]
	v_cvt_pk_bf16_f32 v31, v14, v15
	v_pk_fma_f32 v[14:15], v[66:67], s[90:91], v[20:21] op_sel_hi:[1,0,1]
	v_cvt_pk_bf16_f32 v16, v10, v11
	v_cvt_pk_bf16_f32 v17, v8, v9
	v_cvt_pk_bf16_f32 v12, v12, v13
	v_cvt_pk_bf16_f32 v14, v14, v15
	v_cndmask_b32_e64 v8, v31, v12, s[38:39]
	v_cndmask_b32_e64 v10, v29, v17, s[38:39]
	v_cndmask_b32_e64 v11, v28, v16, s[38:39]
	v_cndmask_b32_e64 v9, v30, v14, s[38:39]
	v_mov_b32_dpp v13, v10 quad_perm:[1,0,3,2] row_mask:0xf bank_mask:0xf bound_ctrl:1
	v_mov_b32_dpp v18, v11 quad_perm:[1,0,3,2] row_mask:0xf bank_mask:0xf bound_ctrl:1
	v_mov_b32_dpp v15, v8 quad_perm:[1,0,3,2] row_mask:0xf bank_mask:0xf bound_ctrl:1
	v_mov_b32_dpp v19, v9 quad_perm:[1,0,3,2] row_mask:0xf bank_mask:0xf bound_ctrl:1
	v_cndmask_b32_e64 v11, v15, v31, s[38:39]
	v_cndmask_b32_e64 v9, v13, v29, s[38:39]
	v_cndmask_b32_e64 v15, v12, v15, s[38:39]
	v_cndmask_b32_e64 v13, v17, v13, s[38:39]
	v_cndmask_b32_e64 v12, v16, v18, s[38:39]
	v_lshl_add_u64 v[16:17], s[44:45], 0, v[184:185]
	v_cndmask_b32_e64 v26, v5, v1, s[38:39]
	v_cndmask_b32_e64 v27, v4, v0, s[38:39]
	v_cndmask_b32_e64 v10, v19, v30, s[38:39]
	v_cndmask_b32_e64 v8, v18, v28, s[38:39]
	v_lshl_add_u64 v[16:17], v[16:17], 0, v[180:181]
	v_cndmask_b32_e64 v24, v7, v3, s[38:39]
	v_cndmask_b32_e64 v14, v14, v19, s[38:39]
	global_store_dwordx4 v[16:17], v[8:11], off nt
	v_mov_b32_e32 v50, 0
	v_mov_b32_e32 v51, 0
	v_mov_b32_e32 v52, 0
	v_mov_b32_e32 v53, 0
	v_mov_b32_e32 v54, 0
	v_mov_b32_e32 v55, 0
	v_mov_b32_e32 v56, 0
	v_mov_b32_e32 v57, 0
	v_mov_b32_e32 v66, 0
	v_mov_b32_e32 v67, 0
	v_mov_b32_e32 v68, 0
	v_mov_b32_e32 v69, 0
	v_mov_b32_e32 v70, 0
	v_mov_b32_e32 v71, 0
	v_mov_b32_e32 v72, 0
	v_mov_b32_e32 v73, 0
	v_mov_b32_e32 v82, 0
	v_mov_b32_e32 v83, 0
	v_mov_b32_e32 v84, 0
	v_mov_b32_e32 v85, 0
	global_store_dwordx4 v[16:17], v[12:15], off offset:2048 nt
	s_nop 0
	v_mov_b32_dpp v8, v27 quad_perm:[1,0,3,2] row_mask:0xf bank_mask:0xf bound_ctrl:1
	v_mov_b32_dpp v9, v26 quad_perm:[1,0,3,2] row_mask:0xf bank_mask:0xf bound_ctrl:1
	v_mov_b32_dpp v10, v25 quad_perm:[1,0,3,2] row_mask:0xf bank_mask:0xf bound_ctrl:1
	v_mov_b32_dpp v11, v24 quad_perm:[1,0,3,2] row_mask:0xf bank_mask:0xf bound_ctrl:1
	v_cndmask_b32_e64 v6, v10, v6, s[38:39]
	v_cndmask_b32_e64 v5, v9, v5, s[38:39]
	v_cndmask_b32_e64 v4, v8, v4, s[38:39]
	v_cndmask_b32_e64 v7, v11, v7, s[38:39]
	v_cndmask_b32_e64 v15, v3, v11, s[38:39]
	v_cndmask_b32_e64 v13, v2, v10, s[38:39]
	v_cndmask_b32_e64 v11, v1, v9, s[38:39]
	v_cndmask_b32_e64 v9, v0, v8, s[38:39]
	v_lshlrev_b32_e32 v0, 16, v4
	v_and_b32_e32 v1, 0xffff0000, v4
	v_lshlrev_b32_e32 v2, 16, v5
	v_and_b32_e32 v3, 0xffff0000, v5
	v_lshlrev_b32_e32 v4, 16, v6
	v_and_b32_e32 v5, 0xffff0000, v6
	v_lshlrev_b32_e32 v6, 16, v7
	v_and_b32_e32 v7, 0xffff0000, v7
	v_lshlrev_b32_e32 v8, 16, v9
	v_and_b32_e32 v9, 0xffff0000, v9
	v_lshlrev_b32_e32 v10, 16, v11
	v_and_b32_e32 v11, 0xffff0000, v11
	v_lshlrev_b32_e32 v14, 16, v15
	v_and_b32_e32 v15, 0xffff0000, v15
	v_pk_fma_f32 v[2:3], v[38:39], s[90:91], v[2:3] op_sel_hi:[1,0,1]
	v_pk_fma_f32 v[0:1], v[36:37], s[90:91], v[0:1] op_sel_hi:[1,0,1]
	v_pk_fma_f32 v[4:5], v[32:33], s[90:91], v[4:5] op_sel_hi:[1,0,1]
	v_lshlrev_b32_e32 v12, 16, v13
	v_and_b32_e32 v13, 0xffff0000, v13
	v_pk_fma_f32 v[6:7], v[34:35], s[90:91], v[6:7] op_sel_hi:[1,0,1]
	v_cvt_pk_bf16_f32 v16, v0, v1
	v_cvt_pk_bf16_f32 v17, v2, v3
	v_cvt_pk_bf16_f32 v18, v4, v5
	v_pk_fma_f32 v[0:1], v[46:47], s[90:91], v[10:11] op_sel_hi:[1,0,1]
	v_pk_fma_f32 v[2:3], v[44:45], s[90:91], v[8:9] op_sel_hi:[1,0,1]
	v_pk_fma_f32 v[4:5], v[42:43], s[90:91], v[14:15] op_sel_hi:[1,0,1]
	v_cvt_pk_bf16_f32 v19, v6, v7
	v_pk_fma_f32 v[6:7], v[40:41], s[90:91], v[12:13] op_sel_hi:[1,0,1]
	v_cvt_pk_bf16_f32 v8, v2, v3
	v_cvt_pk_bf16_f32 v9, v0, v1
	v_cvt_pk_bf16_f32 v4, v4, v5
	v_cvt_pk_bf16_f32 v6, v6, v7
	v_cndmask_b32_e64 v0, v19, v4, s[38:39]
	v_cndmask_b32_e64 v2, v17, v9, s[38:39]
	v_cndmask_b32_e64 v3, v16, v8, s[38:39]
	v_cndmask_b32_e64 v1, v18, v6, s[38:39]
	v_mov_b32_dpp v5, v2 quad_perm:[1,0,3,2] row_mask:0xf bank_mask:0xf bound_ctrl:1
	v_mov_b32_dpp v10, v3 quad_perm:[1,0,3,2] row_mask:0xf bank_mask:0xf bound_ctrl:1
	v_mov_b32_dpp v7, v0 quad_perm:[1,0,3,2] row_mask:0xf bank_mask:0xf bound_ctrl:1
	v_mov_b32_dpp v11, v1 quad_perm:[1,0,3,2] row_mask:0xf bank_mask:0xf bound_ctrl:1
	v_cndmask_b32_e64 v3, v7, v19, s[38:39]
	v_cndmask_b32_e64 v1, v5, v17, s[38:39]
	v_cndmask_b32_e64 v7, v4, v7, s[38:39]
	v_cndmask_b32_e64 v5, v9, v5, s[38:39]
	v_cndmask_b32_e64 v4, v8, v10, s[38:39]
	v_lshl_add_u64 v[8:9], s[44:45], 0, v[182:183]
	v_cndmask_b32_e64 v2, v11, v18, s[38:39]
	v_cndmask_b32_e64 v0, v10, v16, s[38:39]
	v_lshl_add_u64 v[8:9], v[8:9], 0, v[180:181]
	v_cndmask_b32_e64 v6, v6, v11, s[38:39]
	global_store_dwordx4 v[8:9], v[0:3], off nt
	v_mov_b32_e32 v32, 0
	v_mov_b32_e32 v33, 0
	v_mov_b32_e32 v34, 0
	v_mov_b32_e32 v35, 0
	v_mov_b32_e32 v36, 0
	v_mov_b32_e32 v37, 0
	v_mov_b32_e32 v38, 0
	v_mov_b32_e32 v39, 0
	v_mov_b32_e32 v40, 0
	v_mov_b32_e32 v41, 0
	v_mov_b32_e32 v42, 0
	v_mov_b32_e32 v43, 0
	v_mov_b32_e32 v44, 0
	v_mov_b32_e32 v45, 0
	v_mov_b32_e32 v46, 0
	v_mov_b32_e32 v47, 0
	global_store_dwordx4 v[8:9], v[4:7], off offset:2048 nt
	s_cbranch_vccnz .LBB0_515
	s_andn2_b64 vcc, exec, s[42:43]
	s_cbranch_vccnz .LBB0_514
	s_barrier
	s_branch .LBB0_514
